# v76 + SWA item setup: sink-logit load no longer waited before the first K/V tile DMA issue (one memory round trip per SWA item instead of two; sink in v191, vmcnt(2) at end of preheader)
# speedup vs baseline: 1.0015x; 1.0015x over previous
.LBB0_3607:
	s_or_b64 exec, exec, s[4:5]
	v_mov_b32_e32 v0, s59
	s_waitcnt lgkmcnt(0)
	s_barrier
	ds_read_b32 v0, v0
	v_readlane_b32 s2, v254, 55
	v_readlane_b32 s3, v254, 56
	s_xor_b64 s[40:41], s[2:3], -1
	s_waitcnt lgkmcnt(0)
	v_readfirstlane_b32 s69, v0
	s_cmpk_gt_i32 s69, 0x67f
	s_cselect_b64 s[86:87], -1, 0
	s_and_b64 vcc, exec, s[86:87]
	s_barrier
	s_cbranch_vccnz .LBB0_3602
	v_mov_b32_e32 v154, v147
	s_mov_b64 s[6:7], -1
	v_readfirstlane_b32 s33, v154
	s_ashr_i32 s79, s33, 6
	v_and_b32_e32 v153, 63, v154
	s_cmpk_gt_i32 s69, 0x7f
	s_cbranch_scc0 .LBB0_3774
	s_add_i32 s48, s69, 0xfffffd80
	s_cmpk_gt_u32 s48, 0x1ff
	s_mov_b64 s[4:5], -1
	s_cbranch_scc0 .LBB0_3657
	s_cmpk_gt_u32 s69, 0x27f
	s_cbranch_scc0 .LBB0_3635
	s_cmpk_lt_u32 s69, 0x480
	s_cbranch_scc1 .LBB0_3634
	v_readlane_b32 s2, v254, 58
	v_readlane_b32 s3, v254, 59
	s_load_dwordx2 s[4:5], s[2:3], 0x28
	s_add_i32 s0, s69, 0xfffffb80
	s_lshr_b32 s6, s0, 4
	s_sub_i32 s2, 31, s6
	v_readlane_b32 s8, v255, 34
	v_readlane_b32 s9, v255, 35
	s_waitcnt lgkmcnt(0)
	s_add_u32 s7, s4, s8
	s_addc_u32 s8, s5, s9
	s_and_b32 s0, s69, 1
	s_lshl_b32 s4, s0, 2
	s_ashr_i32 s5, s33, 7
	s_lshl_b32 s9, s79, 5
	s_add_i32 s4, s5, s4
	s_lshl_b32 s5, s2, 6
	s_and_b32 s9, s9, 32
	s_or_b32 s5, s9, s5
	s_bfe_u32 s3, s69, 0x30001
	v_and_or_b32 v119, v154, 31, s5
	v_lshl_or_b32 v118, s3, 11, v119
	v_readlane_b32 s10, v254, 60
	v_lshlrev_b32_e32 v0, 10, v118
	v_readlane_b32 s11, v254, 61
	s_lshl_b32 s42, s4, 6
	v_lshrrev_b32_e32 v2, 5, v153
	v_lshl_add_u64 v[4:5], s[10:11], 0, v[0:1]
	s_ashr_i32 s43, s42, 31
	v_lshl_add_u64 v[4:5], s[42:43], 1, v[4:5]
	v_lshlrev_b32_e32 v0, 4, v2
	s_ashr_i32 s5, s4, 31
	v_lshl_add_u64 v[4:5], v[4:5], 0, v[0:1]
	s_lshl_b64 s[4:5], s[4:5], 2
	global_load_dwordx4 v[66:69], v[4:5], off
	global_load_dwordx4 v[70:73], v[4:5], off offset:32
	global_load_dwordx4 v[74:77], v[4:5], off offset:64
	global_load_dwordx4 v[78:81], v[4:5], off offset:96
	s_add_u32 s4, s7, s4
	s_addc_u32 s5, s8, s5
	global_load_dword v191, v1, s[4:5]
	v_sub_u32_e64 v3, 29, s6 clamp
	s_min_u32 s4, s6, 29
	v_readfirstlane_b32 s5, v3
	s_max_u32 s5, s2, s5
	s_add_i32 s4, s4, s5
	s_sub_i32 s10, s4, 28
	s_cmp_lt_u32 s10, 2
	v_readfirstlane_b32 s4, v3
	s_cbranch_scc1 .LBB0_3616
	s_and_b32 s11, s10, -2
	s_add_i32 s5, s4, 1
	s_mov_b32 s6, 0
	s_mov_b32 s12, s11
	s_mov_b64 s[8:9], s[4:5]
	s_mov_b32 s7, s6

.LBB0_3618:
	s_lshl_b32 s3, s3, 19
	v_readlane_b32 s7, v254, 62
	s_add_u32 s7, s7, s3
	v_readlane_b32 s8, v254, 63
	s_addc_u32 s8, s8, 0
	s_lshl_b32 s0, s0, 7
	s_add_u32 s10, s7, s0
	s_addc_u32 s11, s8, 0
	v_readlane_b32 s7, v255, 0
	s_add_u32 s3, s7, s3
	v_readlane_b32 s7, v255, 1
	s_addc_u32 s7, s7, 0
	s_add_u32 s12, s3, s0
	s_addc_u32 s13, s7, 0
	s_ff1_i32_b32 s8, s6
	s_add_i32 s0, s6, -1
	s_and_b32 s3, s0, s6
	s_lshl_b32 s0, s8, 14
	s_add_u32 s6, s12, s0
	s_addc_u32 s7, s13, 0
	v_lshlrev_b32_e32 v0, 8, v153
	v_lshl_add_u64 v[4:5], s[6:7], 0, v[0:1]
	s_lshl_b32 s6, s79, 3
	s_ashr_i32 s7, s6, 31
	s_lshl_b64 s[14:15], s[6:7], 1
	s_lshl_b32 s7, s79, 10
	s_add_i32 s46, s7, 0
	v_lshl_add_u64 v[4:5], v[4:5], 0, s[14:15]
	s_mov_b32 m0, s46
	s_add_u32 s16, s10, s0
	global_load_lds_dwordx4 v[4:5], off
	v_lshlrev_b32_e32 v4, 6, v153
	v_lshlrev_b32_e32 v8, 3, v153
	s_addc_u32 s17, s11, 0
	v_and_b32_e32 v4, 0xf00, v4
	v_mov_b32_e32 v5, v1
	v_and_b32_e32 v122, 24, v8
	v_lshl_add_u64 v[6:7], s[16:17], 0, v[4:5]
	v_lshlrev_b32_e32 v8, 1, v122
	v_mov_b32_e32 v9, v1
	s_lshl_b32 s0, s79, 12
	s_andn2_b32 s6, s6, 31
	v_lshl_add_u64 v[6:7], v[6:7], 0, v[8:9]
	s_and_b32 s92, s0, 0x3000
	s_ashr_i32 s7, s6, 31
	v_lshl_add_u64 v[6:7], v[6:7], 0, s[92:93]
	s_lshl_b64 s[6:7], s[6:7], 1
	v_lshl_add_u64 v[6:7], v[6:7], 0, s[6:7]
	s_add_i32 m0, s46, 0x4000
	v_lshl_add_u64 v[4:5], s[10:11], 0, v[4:5]
	global_load_lds_dwordx4 v[6:7], off
	v_lshl_add_u64 v[4:5], v[4:5], 0, v[8:9]
	v_lshl_add_u64 v[4:5], v[4:5], 0, s[92:93]
	v_lshlrev_b32_e32 v3, 5, v153
	v_lshl_add_u64 v[82:83], v[4:5], 0, s[6:7]
	v_lshl_add_u64 v[4:5], s[12:13], 0, v[0:1]
	v_lshlrev_b32_e32 v0, 4, v153
	v_and_b32_e32 v123, 0x400, v3
	v_and_b32_e32 v124, 0x1f0, v0
	v_bfe_u32 v0, v154, 2, 2
	v_lshrrev_b32_e32 v3, 3, v154
	v_and_or_b32 v0, v3, 4, v0
	v_lshl_add_u64 v[84:85], v[4:5], 0, s[14:15]
	v_lshlrev_b32_e32 v125, 6, v0
	v_lshlrev_b32_e32 v0, 1, v153
	v_lshlrev_b32_e32 v127, 2, v2
	v_mov_b32_e32 v2, v1
	v_mov_b32_e32 v3, v1
	v_mov_b32_e32 v4, v1
	v_mov_b32_e32 v5, v1
	v_mov_b32_e32 v6, v1
	v_mov_b32_e32 v7, v1
	v_mov_b32_e32 v8, v1
	v_mov_b32_e32 v10, v1
	v_mov_b32_e32 v11, v1
	v_mov_b32_e32 v12, v1
	v_mov_b32_e32 v13, v1
	v_mov_b32_e32 v14, v1
	v_mov_b32_e32 v15, v1
	v_mov_b32_e32 v16, v1
	v_mov_b32_e32 v17, v1
	v_mov_b32_e32 v18, v1
	v_mov_b32_e32 v19, v1
	v_mov_b32_e32 v20, v1
	v_mov_b32_e32 v21, v1
	v_mov_b32_e32 v22, v1
	v_mov_b32_e32 v23, v1
	v_mov_b32_e32 v24, v1
	v_mov_b32_e32 v25, v1
	v_mov_b32_e32 v26, v1
	v_mov_b32_e32 v27, v1
	v_mov_b32_e32 v28, v1
	v_mov_b32_e32 v29, v1
	v_mov_b32_e32 v30, v1
	v_mov_b32_e32 v31, v1
	v_cmp_gt_u32_e64 s[4:5], 32, v153
	v_and_b32_e32 v126, 32, v0
	v_mov_b32_e32 v0, v1
	v_mov_b32_e32 v86, 0
	v_mov_b64_e32 v[32:33], v[30:31]
	s_mov_b32 s2, 0
	v_cndmask_b32_e64 v120, 0, 1.0, s[4:5]
	v_mov_b64_e32 v[30:31], v[28:29]
	v_mov_b64_e32 v[28:29], v[26:27]
	v_mov_b64_e32 v[26:27], v[24:25]
	v_mov_b64_e32 v[24:25], v[22:23]
	v_mov_b64_e32 v[22:23], v[20:21]
	v_mov_b64_e32 v[20:21], v[18:19]
	v_mov_b64_e32 v[18:19], v[16:17]
	v_mov_b64_e32 v[16:17], v[14:15]
	v_mov_b64_e32 v[14:15], v[12:13]
	v_mov_b64_e32 v[12:13], v[10:11]
	v_mov_b64_e32 v[10:11], v[8:9]
	v_mov_b64_e32 v[8:9], v[6:7]
	v_mov_b64_e32 v[6:7], v[4:5]
	v_mov_b64_e32 v[4:5], v[2:3]
	v_mov_b64_e32 v[2:3], v[0:1]
	v_mov_b32_e32 v87, v86
	v_mov_b32_e32 v88, v86
	v_mov_b32_e32 v89, v86
	v_mov_b32_e32 v90, v86
	v_mov_b32_e32 v91, v86
	v_mov_b32_e32 v92, v86
	v_mov_b32_e32 v93, v86
	v_mov_b32_e32 v94, v86
	v_mov_b32_e32 v95, v86
	v_mov_b32_e32 v96, v86
	v_mov_b32_e32 v97, v86
	v_mov_b32_e32 v98, v86
	v_mov_b32_e32 v99, v86
	v_mov_b32_e32 v100, v86
	v_mov_b32_e32 v101, v86
	v_mov_b32_e32 v102, v86
	v_mov_b32_e32 v103, v86
	v_mov_b32_e32 v104, v86
	v_mov_b32_e32 v105, v86
	v_mov_b32_e32 v106, v86
	v_mov_b32_e32 v107, v86
	v_mov_b32_e32 v108, v86
	v_mov_b32_e32 v109, v86
	v_mov_b32_e32 v110, v86
	v_mov_b32_e32 v111, v86
	v_mov_b32_e32 v112, v86
	v_mov_b32_e32 v113, v86
	v_mov_b32_e32 v114, v86
	v_mov_b32_e32 v115, v86
	v_mov_b32_e32 v116, v86
	v_mov_b32_e32 v117, v86
	s_waitcnt vmcnt(2)
	v_mul_f32_e32 v121, 0x3fb8aa3b, v191
